# v9 + neighbourhood-attention rel-pos-bias LDS table filled once per workgroup (same head for all its units) instead of per unit
# speedup vs baseline: 1.0076x; 1.0006x over previous
.LBB0_806:
	v_writelane_b32 v255, s8, 27
	s_bfe_u32 s6, s8, 0x30004
	s_cmpk_gt_i32 s8, 0xff
	s_cbranch_scc1 .Lna_tfill_skip
	v_readlane_b32 s8, v255, 19
	v_readlane_b32 s9, v255, 20
	s_and_saveexec_b64 s[2:3], s[8:9]
	s_cbranch_execz .LBB0_811
	v_readlane_b32 s7, v255, 18
	s_or_b32 s7, s6, s7
	s_mov_b32 s24, s12
	s_mov_b64 s[26:27], s[16:17]
	v_readlane_b32 s8, v253, 50
	s_mulk_i32 s7, 0x744
	v_readlane_b32 s18, v253, 60
	v_readlane_b32 s20, v253, 62
	v_readlane_b32 s12, v253, 54
	v_readlane_b32 s16, v253, 58
	v_readlane_b32 s17, v253, 59
	v_readlane_b32 s19, v253, 61
	v_readlane_b32 s21, v253, 63
	s_add_u32 s18, s20, s7
	s_mov_b64 s[16:17], s[26:27]
	s_mov_b32 s12, s24
	s_addc_u32 s19, s21, 0
	s_mov_b64 s[20:21], 0
	v_mov_b32_e32 v0, v229
	v_mov_b32_e32 v1, v220
	v_readlane_b32 s9, v253, 51
	v_readlane_b32 s10, v253, 52
	v_readlane_b32 s11, v253, 53
	v_readlane_b32 s13, v253, 55
	v_readlane_b32 s14, v253, 56
	v_readlane_b32 s15, v253, 57
	v_readlane_b32 s22, v254, 0
	v_readlane_b32 s23, v254, 1
	s_branch .LBB0_809

.Lna_tfill_skip:
	v_readlane_b32 s9, v255, 27
	s_lshr_b32 s7, s9, 4
	s_ashr_i32 s10, s9, 5
	s_bfe_u32 s2, s9, 0x30005
	s_and_b32 s10, s10, -8
	s_and_b32 s20, s7, 1
	v_readlane_b32 s7, v255, 23
	s_or_b32 s2, s10, s2
	s_bfe_u32 s10, s7, 0x40002
	s_lshr_b32 s27, s7, 2
	s_lshl_b32 s7, s10, 2
	s_lshl_b32 s24, s10, 11
	s_lshl_b32 s10, s9, 2
	v_readlane_b32 s8, v255, 25
	s_and_b32 s29, s10, 60
	v_med3_u32 v10, s7, 4, 56
	s_add_i32 s7, s8, s7
	v_med3_u32 v246, s29, 4, 56
	v_readfirstlane_b32 s11, v10
	v_med3_i32 v0, s7, 4, 60
	v_readfirstlane_b32 s10, v246
	s_mul_i32 s13, s11, 0x48000
	v_readfirstlane_b32 s7, v0
	s_ashr_i32 s2, s2, 2
	s_lshl_b32 s10, s10, 6
	s_lshr_b32 s3, s9, 5
	s_add_i32 s26, s13, 0xffee0000
	s_sub_i32 s7, s11, s7
	s_mul_i32 s14, s2, 0x1100
	s_add_i32 s13, s10, 0xffffff00
	s_lshl_b32 s10, s29, 6
	s_mul_hi_i32 s11, s2, 0x1100
	s_add_u32 s18, s14, s10
	s_addc_u32 s19, s11, 0
	s_mul_i32 s10, s19, 0x1200
	s_mul_hi_u32 s11, s18, 0x1200
	s_add_i32 s11, s11, s10
	s_mul_i32 s10, s18, 0x1200
	v_readlane_b32 s8, v255, 16
	s_add_u32 s10, s8, s10
	v_readlane_b32 s9, v255, 17
	s_addc_u32 s11, s9, s11
	s_lshl_b32 s14, s6, 6
	s_lshl_b32 s6, s6, 7
	s_add_u32 s21, s10, s6
	s_addc_u32 s23, s11, 0
	s_mul_i32 s15, s2, 0x1320000
	v_writelane_b32 v255, s14, 29
	s_mul_hi_i32 s14, s2, 0x1320000
	s_add_u32 s2, s8, s15
	s_addc_u32 s11, s9, s14
	s_add_u32 s10, s2, s6
	s_addc_u32 s11, s11, 0
	v_readlane_b32 s8, v255, 8
	v_lshl_add_u64 v[0:1], s[10:11], 0, v[172:173]
	v_readlane_b32 s9, v255, 9
	v_readlane_b32 s2, v255, 3
	s_add_u32 s22, s21, s2
	v_lshl_add_u64 v[66:67], s[8:9], 1, v[0:1]
	v_readlane_b32 s8, v255, 10
	v_readlane_b32 s2, v255, 14
	v_lshl_add_u64 v[0:1], s[10:11], 0, v[174:175]
	v_readlane_b32 s9, v255, 11
	s_addc_u32 s23, s23, s2
	v_mov_b32_e32 v209, v115
	v_lshl_add_u64 v[0:1], s[8:9], 1, v[0:1]
	s_mov_b64 s[10:11], 0x1200a00
	v_lshl_add_u64 v[212:213], v[0:1], 0, v[208:209]
	v_lshl_add_u64 v[0:1], v[66:67], 0, s[10:11]
	s_mov_b64 s[10:11], 0x1200e00
	s_cmp_lg_u32 0, -1
	s_mov_b32 s2, m0
	s_mov_b32 m0, s34
	s_nop 0
	global_load_lds_dwordx4 v[0:1], off
	s_mov_b32 m0, s2
	v_lshl_add_u64 v[0:1], v[212:213], 0, s[10:11]
	s_mov_b64 s[10:11], 0x1248a00
	s_cselect_b32 s21, 0, 0
	s_mov_b32 s2, m0
	s_mov_b32 m0, s35
	s_nop 0
	global_load_lds_dwordx4 v[0:1], off
	s_mov_b32 m0, s2
	v_lshl_add_u64 v[0:1], v[66:67], 0, s[10:11]
	s_add_i32 s21, s21, s12
	s_add_i32 s2, s21, 0x2000
	s_mov_b32 s6, m0
	s_mov_b32 m0, s2
	s_nop 0
	global_load_lds_dwordx4 v[0:1], off
	s_mov_b32 m0, s6
	v_lshl_add_u64 v[0:1], v[176:177], 1, s[22:23]
	v_mov_b32_e32 v211, v115
	v_lshl_add_u64 v[0:1], v[0:1], 0, v[210:211]
	flat_load_dwordx4 v[128:131], v[0:1] offset:1536
	flat_load_dwordx4 v[124:127], v[0:1] offset:1568
	flat_load_dwordx4 v[120:123], v[0:1] offset:1600
	flat_load_dwordx4 v[116:119], v[0:1] offset:1632
	v_mov_b32_e32 v0, v115
	s_mov_b64 s[10:11], 0x1290a00
	v_lshl_add_u64 v[2:3], v[66:67], 0, s[10:11]
	s_add_i32 s2, s21, 0x4000
	s_mov_b32 s6, m0
	s_mov_b32 m0, s2
	s_nop 0
	global_load_lds_dwordx4 v[2:3], off
	s_mov_b32 m0, s6
	s_waitcnt vmcnt(3) lgkmcnt(0)
	s_barrier
	ds_read_b128 v[2:5], v221
	ds_read_b128 v[6:9], v221 offset:512
	v_lshlrev_b32_e32 v1, 9, v10
	s_mov_b64 s[22:23], 0x12d8a00
	s_add_i32 s21, s21, 0x8000
	s_and_b32 s3, s3, 3
	s_lshl_b32 s20, s20, 7
	s_lshl_b32 s3, s3, 8
	s_or_b32 s20, s3, s20
	s_or_b32 s3, s15, s20
	v_mov_b32_e32 v14, v0
	v_mov_b32_e32 v15, v0
	v_subrev_u32_e32 v216, s24, v1
	v_mov_b32_e32 v1, v0
	s_mov_b32 s11, 1
	s_mov_b32 s2, 0
	s_movk_i32 s6, 0x2000
	s_movk_i32 s10, 0x4000
	s_waitcnt vmcnt(0) lgkmcnt(0)
	v_mfma_f32_32x32x16_bf16 v[32:47], v[2:5], v[128:131], 0
	v_add_u32_e32 v217, v230, v216
	v_mov_b32_e32 v211, 0
	v_mfma_f32_32x32x16_bf16 v[16:31], v[6:9], v[128:131], 0
	ds_read_b128 v[2:5], v221 offset:2048
	ds_read_b128 v[6:9], v221 offset:2560
	s_waitcnt lgkmcnt(1)
	v_mfma_f32_32x32x16_bf16 v[32:47], v[2:5], v[124:127], v[32:47]
	ds_read_b128 v[2:5], v221 offset:4096
	s_waitcnt lgkmcnt(1)
	v_mfma_f32_32x32x16_bf16 v[16:31], v[6:9], v[124:127], v[16:31]
	ds_read_b128 v[6:9], v221 offset:4608
	ds_read_b128 v[48:51], v221 offset:6656
	ds_read_b128 v[10:13], v221 offset:6144
	s_waitcnt lgkmcnt(3)
	v_mfma_f32_32x32x16_bf16 v[32:47], v[2:5], v[120:123], v[32:47]
	v_mov_b32_e32 v2, v0
	v_mov_b32_e32 v3, v0
	v_mov_b32_e32 v4, v0
	v_mov_b32_e32 v5, v0
	s_waitcnt lgkmcnt(2)
	v_mfma_f32_32x32x16_bf16 v[16:31], v[6:9], v[120:123], v[16:31]
	v_mov_b32_e32 v6, v0
	v_mov_b32_e32 v7, v0
	v_mov_b32_e32 v8, v0
	v_mov_b32_e32 v9, v0
	s_waitcnt lgkmcnt(0)
	v_mfma_f32_32x32x16_bf16 v[32:47], v[10:13], v[116:119], v[32:47]
	v_mov_b32_e32 v10, v0
	v_mov_b32_e32 v11, v0
	v_mov_b32_e32 v12, v0
	v_mov_b32_e32 v13, v0
	v_mfma_f32_32x32x16_bf16 v[16:31], v[48:51], v[116:119], v[16:31]
	s_nop 15
	s_nop 7
	s_waitcnt vmcnt(0) lgkmcnt(0)
	s_barrier
	s_nop 0
	v_max3_f32 v48, v32, v33, v16
	v_max3_f32 v49, v34, v35, v17
	s_nop 0
	v_max3_f32 v48, v48, v18, v19
	v_max3_f32 v49, v49, v38, v39
	s_nop 0
	v_max3_f32 v48, v48, v36, v37
	v_max3_f32 v49, v49, v22, v23
	s_nop 0
	v_max3_f32 v48, v48, v20, v21
	v_max3_f32 v49, v49, v42, v43
	s_nop 0
	v_max3_f32 v48, v48, v40, v41
	v_max3_f32 v49, v49, v26, v27
	s_nop 0
	v_max3_f32 v48, v48, v24, v25
	v_max3_f32 v49, v49, v46, v47
	s_nop 0
	v_max3_f32 v48, v48, v44, v45
	v_max3_f32 v49, v49, v30, v31
	s_nop 0
	v_max3_f32 v48, v48, v28, v29
	s_nop 0
	v_max_f32_e32 v48, v48, v49
	s_nop 0
	v_mov_b32_e32 v49, v48
	s_nop 1
	v_permlane32_swap_b32_e32 v48, v49
	v_max_f32_e32 v48, v48, v49
	s_nop 0
	v_sub_f32_e32 v16, v16, v48
	v_sub_f32_e32 v17, v17, v48
	v_add_f32_e32 v209, v115, v48
	v_sub_f32_e32 v32, v32, v48
	v_sub_f32_e32 v33, v33, v48
	v_sub_f32_e32 v34, v34, v48
	v_sub_f32_e32 v18, v18, v48
	v_sub_f32_e32 v35, v35, v48
	v_sub_f32_e32 v19, v19, v48
	v_sub_f32_e32 v36, v36, v48
	v_sub_f32_e32 v20, v20, v48
	v_sub_f32_e32 v37, v37, v48
	v_sub_f32_e32 v21, v21, v48
	v_sub_f32_e32 v38, v38, v48
	v_sub_f32_e32 v22, v22, v48
	v_sub_f32_e32 v39, v39, v48
	v_sub_f32_e32 v23, v23, v48
	v_sub_f32_e32 v40, v40, v48
	v_sub_f32_e32 v24, v24, v48
	v_sub_f32_e32 v41, v41, v48
	v_sub_f32_e32 v25, v25, v48
	v_sub_f32_e32 v42, v42, v48
	v_sub_f32_e32 v26, v26, v48
	v_sub_f32_e32 v43, v43, v48
	v_sub_f32_e32 v27, v27, v48
	v_sub_f32_e32 v44, v44, v48
	v_sub_f32_e32 v28, v28, v48
	v_sub_f32_e32 v45, v45, v48
	v_sub_f32_e32 v29, v29, v48
	v_sub_f32_e32 v46, v46, v48
	v_sub_f32_e32 v30, v30, v48
	v_sub_f32_e32 v47, v47, v48
	v_sub_f32_e32 v31, v31, v48
	s_nop 0
	v_exp_f32_e32 v48, v16
	v_exp_f32_e32 v49, v17
	v_lshl_add_u64 v[16:17], v[66:67], 0, s[22:23]
	s_mov_b32 s22, m0
	s_mov_b32 m0, s34
	s_nop 0
	global_load_lds_dwordx4 v[16:17], off
	s_mov_b32 m0, s22
	s_mov_b64 s[22:23], 0x1248e00
	v_lshl_add_u64 v[16:17], v[212:213], 0, s[22:23]
	s_mov_b32 s22, m0
	s_mov_b32 m0, s21
	s_nop 0
	global_load_lds_dwordx4 v[16:17], off
	s_mov_b32 m0, s22
	ds_read_b128 v[70:73], v221 offset:8192
	ds_read_b128 v[66:69], v221 offset:8704
	ds_read_b128 v[152:155], v221 offset:10240
	ds_read_b128 v[148:151], v221 offset:10752
	ds_read_b128 v[144:147], v221 offset:12288
	ds_read_b128 v[140:143], v221 offset:12800
	ds_read_b128 v[136:139], v221 offset:14336
	ds_read_b128 v[132:135], v221 offset:14848
	v_exp_f32_e32 v32, v32
	v_exp_f32_e32 v33, v33
	v_exp_f32_e32 v34, v34
	v_exp_f32_e32 v35, v35
	v_exp_f32_e32 v36, v36
	v_exp_f32_e32 v37, v37
	v_exp_f32_e32 v38, v38
	v_exp_f32_e32 v39, v39
	v_exp_f32_e32 v40, v40
	v_exp_f32_e32 v41, v41
	v_exp_f32_e32 v42, v42
	v_exp_f32_e32 v43, v43
	v_exp_f32_e32 v44, v44
	v_exp_f32_e32 v45, v45
	v_exp_f32_e32 v46, v46
	v_exp_f32_e32 v47, v47
	v_exp_f32_e32 v50, v18
	v_exp_f32_e32 v51, v19
	v_exp_f32_e32 v52, v20
	v_exp_f32_e32 v53, v21
	v_exp_f32_e32 v54, v22
	v_exp_f32_e32 v55, v23
	v_exp_f32_e32 v56, v24
	v_exp_f32_e32 v57, v25
	v_exp_f32_e32 v58, v26
	v_exp_f32_e32 v59, v27
	v_exp_f32_e32 v60, v28
	v_exp_f32_e32 v61, v29
	v_exp_f32_e32 v62, v30
	v_exp_f32_e32 v63, v31
	s_waitcnt vmcnt(2) lgkmcnt(0)
	s_barrier
	s_add_u32 s22, s3, s26
	s_addc_u32 s23, s14, 0
	v_mov_b64_e32 v[30:31], v[14:15]
	s_mov_b32 s21, s31
	v_lshl_add_u64 v[214:215], v[188:189], 0, s[22:23]
	s_mov_b64 s[22:23], 0x10c0
	v_mov_b64_e32 v[28:29], v[12:13]
	v_mov_b64_e32 v[26:27], v[10:11]
	v_mov_b64_e32 v[24:25], v[8:9]
	v_mov_b64_e32 v[22:23], v[6:7]
	v_mov_b64_e32 v[20:21], v[4:5]
	v_mov_b64_e32 v[18:19], v[2:3]
	v_mov_b64_e32 v[16:17], v[0:1]
